# speedup vs baseline: 1.0799x; 1.0094x over previous
.LBB2_6:
	s_waitcnt vmcnt(2)
	v_cndmask_b32_e64 v78, v47, v43, s[4:5]
	v_cndmask_b32_e64 v102, v48, v44, s[4:5]
	v_sub_u32_e32 v97, v102, v78
	v_med3_i32 v2, v97, 1, 8
	v_add_u32_e32 v2, -1, v2
	v_and_or_b32 v2, v2, 7, v82
	v_lshlrev_b32_e32 v2, 2, v2
	s_waitcnt vmcnt(0)
	v_cndmask_b32_e64 v10, v49, v45, s[4:5]
	ds_bpermute_b32 v11, v2, v10
	v_add_u32_e32 v96, s2, v1
	v_cndmask_b32_e64 v52, v46, v42, s[4:5]
	v_cmp_gt_u32_e32 vcc, 56, v96
	v_cmp_lt_i32_e64 s[2:3], -1, v52
	s_and_b64 s[6:7], vcc, s[2:3]
	v_mov_b64_e32 v[2:3], 0
	v_mov_b64_e32 v[4:5], 0
	s_and_saveexec_b64 s[0:1], s[6:7]
	s_cbranch_execz .LBB2_8
	v_lshlrev_b64 v[2:3], 7, v[52:53]
	v_lshl_add_u64 v[2:3], v[58:59], 0, v[2:3]
	global_load_dwordx4 v[2:5], v[2:3], off
.LBB2_8:
	s_or_b64 exec, exec, s[0:1]
	v_cmp_gt_i32_e64 s[6:7], 1, v97
	v_cmp_lt_i32_e64 s[0:1], 0, v97
	v_mov_b64_e32 v[6:7], 0
	v_mov_b64_e32 v[8:9], 0
	s_and_saveexec_b64 s[10:11], s[0:1]
	s_cbranch_execz .LBB2_10
	v_ashrrev_i32_e32 v7, 31, v52
	v_mov_b32_e32 v6, v52
	v_lshlrev_b64 v[6:7], 7, v[6:7]
	v_lshl_add_u64 v[6:7], v[60:61], 0, v[6:7]
	global_load_dwordx4 v[6:9], v[6:7], off nt

.LBB2_22:
	s_or_saveexec_b64 s[2:3], s[4:5]
	v_mov_b64_e32 v[18:19], 0
	v_mov_b64_e32 v[20:21], 0
	v_mov_b64_e32 v[22:23], 0
	v_mov_b64_e32 v[24:25], 0
	v_mov_b64_e32 v[14:15], 0
	v_mov_b64_e32 v[16:17], 0
	s_xor_b64 exec, exec, s[2:3]
	s_cbranch_execz .LBB2_24
	v_cvt_f32_u32_e32 v26, v97
	v_mov_b32_e32 v28, 0x3727c5ac
	v_rcp_iflag_f32_e32 v26, v26
	v_pk_add_f16 v22, v6, v52
	v_pk_add_f16 v23, v7, v99
	v_pk_add_f16 v24, v8, v98
	v_pk_add_f16 v25, v9, v103
	v_pk_add_f16 v18, v6, v100
	v_pk_add_f16 v19, v7, v101
	v_pk_add_f16 v20, v8, v105
	v_pk_add_f16 v21, v9, v104
	v_pk_mul_f32 v[30:31], v[26:27], v[72:73] op_sel_hi:[0,1]
	v_pk_mul_f32 v[32:33], v[26:27], v[76:77] op_sel_hi:[0,1]
	v_cvt_f32_f16_e32 v34, v6
	v_cvt_f32_f16_sdwa v35, v6 dst_sel:DWORD dst_unused:UNUSED_PAD src0_sel:WORD_1
	v_pk_fma_f32 v[32:33], v[30:31], v[30:31], v[32:33] neg_lo:[1,0,0] neg_hi:[1,0,0]
	v_pk_add_f32 v[34:35], v[34:35], v[30:31]
	v_max_f32_e32 v32, 0, v32
	v_max_f32_e32 v33, 0, v33
	v_pk_add_f32 v[32:33], v[32:33], v[28:29] op_sel_hi:[1,0]
	v_sqrt_f32_e32 v32, v32
	v_sqrt_f32_e32 v33, v33
	v_cvt_pk_f16_f32 v14, v34, v35
	v_cvt_pk_f16_f32 v10, v32, v33
	v_pk_mul_f32 v[36:37], v[26:27], v[70:71] op_sel_hi:[0,1]
	v_pk_mul_f32 v[38:39], v[26:27], v[74:75] op_sel_hi:[0,1]
	v_cvt_f32_f16_e32 v40, v7
	v_cvt_f32_f16_sdwa v41, v7 dst_sel:DWORD dst_unused:UNUSED_PAD src0_sel:WORD_1
	v_pk_fma_f32 v[38:39], v[36:37], v[36:37], v[38:39] neg_lo:[1,0,0] neg_hi:[1,0,0]
	v_pk_add_f32 v[40:41], v[40:41], v[36:37]
	v_max_f32_e32 v38, 0, v38
	v_max_f32_e32 v39, 0, v39
	v_pk_add_f32 v[38:39], v[38:39], v[28:29] op_sel_hi:[1,0]
	v_sqrt_f32_e32 v38, v38
	v_sqrt_f32_e32 v39, v39
	v_cvt_pk_f16_f32 v15, v40, v41
	v_cvt_pk_f16_f32 v11, v38, v39
	v_pk_mul_f32 v[30:31], v[26:27], v[64:65] op_sel_hi:[0,1]
	v_pk_mul_f32 v[32:33], v[26:27], v[68:69] op_sel_hi:[0,1]
	v_cvt_f32_f16_e32 v34, v8
	v_cvt_f32_f16_sdwa v35, v8 dst_sel:DWORD dst_unused:UNUSED_PAD src0_sel:WORD_1
	v_pk_fma_f32 v[32:33], v[30:31], v[30:31], v[32:33] neg_lo:[1,0,0] neg_hi:[1,0,0]
	v_pk_add_f32 v[34:35], v[34:35], v[30:31]
	v_max_f32_e32 v32, 0, v32
	v_max_f32_e32 v33, 0, v33
	v_pk_add_f32 v[32:33], v[32:33], v[28:29] op_sel_hi:[1,0]
	v_sqrt_f32_e32 v32, v32
	v_sqrt_f32_e32 v33, v33
	v_cvt_pk_f16_f32 v16, v34, v35
	v_cvt_pk_f16_f32 v12, v32, v33
	v_pk_mul_f32 v[36:37], v[26:27], v[62:63] op_sel_hi:[0,1]
	v_pk_mul_f32 v[38:39], v[26:27], v[66:67] op_sel_hi:[0,1]
	v_cvt_f32_f16_e32 v40, v9
	v_cvt_f32_f16_sdwa v41, v9 dst_sel:DWORD dst_unused:UNUSED_PAD src0_sel:WORD_1
	v_pk_fma_f32 v[38:39], v[36:37], v[36:37], v[38:39] neg_lo:[1,0,0] neg_hi:[1,0,0]
	v_pk_add_f32 v[40:41], v[40:41], v[36:37]
	v_max_f32_e32 v38, 0, v38
	v_max_f32_e32 v39, 0, v39
	v_pk_add_f32 v[38:39], v[38:39], v[28:29] op_sel_hi:[1,0]
	v_sqrt_f32_e32 v38, v38
	v_sqrt_f32_e32 v39, v39
	v_cvt_pk_f16_f32 v17, v40, v41
	v_cvt_pk_f16_f32 v13, v38, v39
